# attention softmax: score minus row max in place with packed f32 adds (2 per instruction, max broadcast + negated by operand modifiers), v_exp reads the score register directly
# baseline (speedup 1.0000x reference)
.LBB0_471:
	s_mov_b32 s4, 0xff800000
	v_cndmask_b32_e64 v70, v81, v226, s[78:79]
	v_max3_f32 v33, v18, v97, v20
	v_max3_f32 v33, v33, v19, v22
	v_max3_f32 v33, v33, v21, v24
	v_max3_f32 v33, v33, v23, v26
	v_max3_f32 v33, v33, v25, v28
	v_max3_f32 v33, v33, v27, v31
	v_max3_f32 v33, v33, v29, v30
	v_max3_f32 v33, v33, v32, v3
	v_max3_f32 v33, v33, v2, v5
	v_max3_f32 v33, v33, v4, v7
	v_max3_f32 v33, v33, v6, v9
	v_max3_f32 v33, v33, v8, v11
	v_max3_f32 v33, v33, v10, v13
	v_max3_f32 v33, v33, v12, v15
	v_max3_f32 v33, v33, v14, v17
	v_max3_f32 v33, v33, v16, v35
	v_max3_f32 v33, v33, v34, v37
	v_max3_f32 v33, v33, v36, v39
	v_max3_f32 v33, v33, v38, v41
	v_max3_f32 v33, v33, v40, v43
	v_max3_f32 v33, v33, v42, v45
	v_max3_f32 v33, v33, v44, v47
	v_max3_f32 v33, v33, v46, v49
	v_max3_f32 v33, v33, v48, v51
	v_max3_f32 v33, v33, v50, v53
	v_max3_f32 v33, v33, v52, v55
	v_max3_f32 v33, v33, v54, v57
	v_max3_f32 v33, v33, v56, v59
	v_max3_f32 v33, v33, v58, v61
	v_max3_f32 v33, v33, v60, v63
	v_max3_f32 v33, v33, v62, v65
	v_max3_f32 v33, v33, v64, v83
	v_max3_f32 v33, v33, v82, v85
	v_max3_f32 v33, v33, v84, v87
	v_max3_f32 v33, v33, v86, v89
	v_max3_f32 v33, v33, v88, v91
	v_max3_f32 v33, v33, v90, v93
	v_max3_f32 v33, v33, v92, v95
	v_max3_f32 v33, v33, v94, v70
	v_max_f32_e32 v33, v33, v96
	v_and_b32_e32 v67, 64, v209
	v_xor_b32_e32 v66, 32, v209
	v_add_u32_e32 v67, 64, v67
	v_cmp_lt_i32_e32 vcc, v66, v67
	s_nop 1
	v_cndmask_b32_e32 v66, v209, v66, vcc
	v_lshlrev_b32_e32 v118, 2, v66
	ds_bpermute_b32 v66, v118, v33
	s_waitcnt lgkmcnt(0)
	v_max_f32_e32 v66, v33, v66
	v_pk_add_f32 v[2:3], v[2:3], v[66:67] op_sel_hi:[1,0] neg_lo:[0,1] neg_hi:[0,1]
	v_pk_add_f32 v[4:5], v[4:5], v[66:67] op_sel_hi:[1,0] neg_lo:[0,1] neg_hi:[0,1]
	v_pk_add_f32 v[6:7], v[6:7], v[66:67] op_sel_hi:[1,0] neg_lo:[0,1] neg_hi:[0,1]
	v_pk_add_f32 v[8:9], v[8:9], v[66:67] op_sel_hi:[1,0] neg_lo:[0,1] neg_hi:[0,1]
	v_pk_add_f32 v[10:11], v[10:11], v[66:67] op_sel_hi:[1,0] neg_lo:[0,1] neg_hi:[0,1]
	v_pk_add_f32 v[12:13], v[12:13], v[66:67] op_sel_hi:[1,0] neg_lo:[0,1] neg_hi:[0,1]
	v_pk_add_f32 v[14:15], v[14:15], v[66:67] op_sel_hi:[1,0] neg_lo:[0,1] neg_hi:[0,1]
	v_pk_add_f32 v[16:17], v[16:17], v[66:67] op_sel_hi:[1,0] neg_lo:[0,1] neg_hi:[0,1]
	v_pk_add_f32 v[18:19], v[18:19], v[66:67] op_sel_hi:[1,0] neg_lo:[0,1] neg_hi:[0,1]
	v_pk_add_f32 v[20:21], v[20:21], v[66:67] op_sel_hi:[1,0] neg_lo:[0,1] neg_hi:[0,1]
	v_pk_add_f32 v[22:23], v[22:23], v[66:67] op_sel_hi:[1,0] neg_lo:[0,1] neg_hi:[0,1]
	v_pk_add_f32 v[24:25], v[24:25], v[66:67] op_sel_hi:[1,0] neg_lo:[0,1] neg_hi:[0,1]
	v_pk_add_f32 v[26:27], v[26:27], v[66:67] op_sel_hi:[1,0] neg_lo:[0,1] neg_hi:[0,1]
	v_pk_add_f32 v[28:29], v[28:29], v[66:67] op_sel_hi:[1,0] neg_lo:[0,1] neg_hi:[0,1]
	v_pk_add_f32 v[30:31], v[30:31], v[66:67] op_sel_hi:[1,0] neg_lo:[0,1] neg_hi:[0,1]
	v_pk_add_f32 v[34:35], v[34:35], v[66:67] op_sel_hi:[1,0] neg_lo:[0,1] neg_hi:[0,1]
	v_pk_add_f32 v[36:37], v[36:37], v[66:67] op_sel_hi:[1,0] neg_lo:[0,1] neg_hi:[0,1]
	v_pk_add_f32 v[38:39], v[38:39], v[66:67] op_sel_hi:[1,0] neg_lo:[0,1] neg_hi:[0,1]
	v_pk_add_f32 v[40:41], v[40:41], v[66:67] op_sel_hi:[1,0] neg_lo:[0,1] neg_hi:[0,1]
	v_pk_add_f32 v[42:43], v[42:43], v[66:67] op_sel_hi:[1,0] neg_lo:[0,1] neg_hi:[0,1]
	v_pk_add_f32 v[44:45], v[44:45], v[66:67] op_sel_hi:[1,0] neg_lo:[0,1] neg_hi:[0,1]
	v_pk_add_f32 v[46:47], v[46:47], v[66:67] op_sel_hi:[1,0] neg_lo:[0,1] neg_hi:[0,1]
	v_pk_add_f32 v[48:49], v[48:49], v[66:67] op_sel_hi:[1,0] neg_lo:[0,1] neg_hi:[0,1]
	v_pk_add_f32 v[50:51], v[50:51], v[66:67] op_sel_hi:[1,0] neg_lo:[0,1] neg_hi:[0,1]
	v_pk_add_f32 v[52:53], v[52:53], v[66:67] op_sel_hi:[1,0] neg_lo:[0,1] neg_hi:[0,1]
	v_pk_add_f32 v[54:55], v[54:55], v[66:67] op_sel_hi:[1,0] neg_lo:[0,1] neg_hi:[0,1]
	v_pk_add_f32 v[56:57], v[56:57], v[66:67] op_sel_hi:[1,0] neg_lo:[0,1] neg_hi:[0,1]
	v_pk_add_f32 v[58:59], v[58:59], v[66:67] op_sel_hi:[1,0] neg_lo:[0,1] neg_hi:[0,1]
	v_pk_add_f32 v[60:61], v[60:61], v[66:67] op_sel_hi:[1,0] neg_lo:[0,1] neg_hi:[0,1]
	v_pk_add_f32 v[62:63], v[62:63], v[66:67] op_sel_hi:[1,0] neg_lo:[0,1] neg_hi:[0,1]
	v_pk_add_f32 v[64:65], v[64:65], v[66:67] op_sel_hi:[1,0] neg_lo:[0,1] neg_hi:[0,1]
	v_pk_add_f32 v[82:83], v[82:83], v[66:67] op_sel_hi:[1,0] neg_lo:[0,1] neg_hi:[0,1]
	v_pk_add_f32 v[84:85], v[84:85], v[66:67] op_sel_hi:[1,0] neg_lo:[0,1] neg_hi:[0,1]
	v_pk_add_f32 v[86:87], v[86:87], v[66:67] op_sel_hi:[1,0] neg_lo:[0,1] neg_hi:[0,1]
	v_pk_add_f32 v[88:89], v[88:89], v[66:67] op_sel_hi:[1,0] neg_lo:[0,1] neg_hi:[0,1]
	v_pk_add_f32 v[90:91], v[90:91], v[66:67] op_sel_hi:[1,0] neg_lo:[0,1] neg_hi:[0,1]
	v_pk_add_f32 v[92:93], v[92:93], v[66:67] op_sel_hi:[1,0] neg_lo:[0,1] neg_hi:[0,1]
	v_pk_add_f32 v[94:95], v[94:95], v[66:67] op_sel_hi:[1,0] neg_lo:[0,1] neg_hi:[0,1]
	v_pk_add_f32 v[96:97], v[96:97], v[66:67] op_sel_hi:[1,0] neg_lo:[0,1] neg_hi:[0,1]
	v_sub_f32_e32 v32, v32, v66
	v_sub_f32_e32 v70, v70, v66
	v_exp_f32_e32 v33, v97
	v_exp_f32_e32 v18, v18
	v_exp_f32_e32 v19, v19
	v_exp_f32_e32 v20, v20
	v_add_f32_e32 v67, 0, v33
	v_exp_f32_e32 v21, v21
	v_add_f32_e32 v67, v18, v67
	v_exp_f32_e32 v22, v22
	v_add_f32_e32 v67, v19, v67
	v_exp_f32_e32 v23, v23
	v_add_f32_e32 v67, v20, v67
	v_exp_f32_e32 v24, v24
	v_add_f32_e32 v67, v21, v67
	v_exp_f32_e32 v119, v25
	v_add_f32_e32 v67, v22, v67
	v_exp_f32_e32 v120, v26
	v_add_f32_e32 v67, v23, v67
	v_exp_f32_e32 v121, v27
	v_add_f32_e32 v25, v24, v67
	v_exp_f32_e32 v122, v28
	v_add_f32_e32 v25, v119, v25
	v_exp_f32_e32 v123, v29
	v_add_f32_e32 v25, v120, v25
	v_exp_f32_e32 v124, v31
	v_add_f32_e32 v25, v121, v25
	v_exp_f32_e32 v125, v32
	v_add_f32_e32 v25, v122, v25
	v_exp_f32_e32 v126, v30
	v_add_f32_e32 v25, v123, v25
	v_exp_f32_e32 v103, v2
	v_add_f32_e32 v25, v124, v25
	v_exp_f32_e32 v106, v3
	v_add_f32_e32 v25, v125, v25
	v_exp_f32_e32 v107, v4
	v_add_f32_e32 v2, v126, v25
	v_exp_f32_e32 v110, v5
	v_add_f32_e32 v2, v103, v2
	v_exp_f32_e32 v111, v6
	v_add_f32_e32 v2, v106, v2
	v_exp_f32_e32 v114, v7
	v_add_f32_e32 v2, v107, v2
	v_exp_f32_e32 v115, v8
	v_add_f32_e32 v2, v110, v2
	v_exp_f32_e32 v117, v9
	v_add_f32_e32 v2, v111, v2
	v_exp_f32_e32 v102, v10
	v_add_f32_e32 v2, v114, v2
	v_exp_f32_e32 v104, v11
	v_add_f32_e32 v2, v115, v2
	v_exp_f32_e32 v105, v12
	v_add_f32_e32 v2, v117, v2
	v_exp_f32_e32 v108, v13
	v_add_f32_e32 v2, v102, v2
	v_exp_f32_e32 v109, v14
	v_add_f32_e32 v2, v104, v2
	v_exp_f32_e32 v112, v15
	v_add_f32_e32 v2, v105, v2
	v_exp_f32_e32 v113, v16
	v_add_f32_e32 v2, v108, v2
	v_exp_f32_e32 v116, v17
	v_add_f32_e32 v2, v109, v2
	v_exp_f32_e32 v72, v34
	v_add_f32_e32 v2, v112, v2
	v_exp_f32_e32 v75, v35
	v_add_f32_e32 v2, v113, v2
	v_exp_f32_e32 v76, v36
	v_add_f32_e32 v2, v116, v2
	v_exp_f32_e32 v79, v37
	v_add_f32_e32 v2, v72, v2
	v_exp_f32_e32 v80, v38
	v_add_f32_e32 v2, v75, v2
	v_exp_f32_e32 v98, v39
	v_add_f32_e32 v2, v76, v2
	v_exp_f32_e32 v99, v40
	v_add_f32_e32 v2, v79, v2
	v_exp_f32_e32 v101, v41
	v_add_f32_e32 v2, v80, v2
	v_exp_f32_e32 v71, v42
	v_add_f32_e32 v2, v98, v2
	v_exp_f32_e32 v73, v43
	v_add_f32_e32 v2, v99, v2
	v_exp_f32_e32 v74, v44
	v_add_f32_e32 v2, v101, v2
	v_exp_f32_e32 v77, v45
	v_add_f32_e32 v2, v71, v2
	v_exp_f32_e32 v78, v46
	v_add_f32_e32 v2, v73, v2
	v_exp_f32_e32 v81, v47
	v_add_f32_e32 v2, v74, v2
	v_exp_f32_e32 v97, v48
	v_add_f32_e32 v2, v77, v2
	v_exp_f32_e32 v100, v49
	v_add_f32_e32 v2, v78, v2
	v_exp_f32_e32 v41, v50
	v_add_f32_e32 v2, v81, v2
	v_exp_f32_e32 v46, v51
	v_add_f32_e32 v2, v97, v2
	v_exp_f32_e32 v47, v52
	v_add_f32_e32 v2, v100, v2
	v_exp_f32_e32 v53, v53
	v_add_f32_e32 v2, v41, v2
	v_exp_f32_e32 v54, v54
	v_add_f32_e32 v2, v46, v2
	v_exp_f32_e32 v67, v55
	v_add_f32_e32 v2, v47, v2
	v_exp_f32_e32 v68, v56
	v_add_f32_e32 v2, v53, v2
	v_exp_f32_e32 v69, v57
	v_add_f32_e32 v2, v54, v2
	v_exp_f32_e32 v38, v58
	v_add_f32_e32 v2, v67, v2
	v_exp_f32_e32 v44, v59
	v_add_f32_e32 v2, v68, v2
	v_exp_f32_e32 v45, v60
	v_add_f32_e32 v2, v69, v2
	v_exp_f32_e32 v51, v61
	v_add_f32_e32 v2, v38, v2
	v_exp_f32_e32 v52, v62
	v_add_f32_e32 v2, v44, v2
	v_exp_f32_e32 v57, v63
	v_add_f32_e32 v2, v45, v2
	v_exp_f32_e32 v58, v64
	v_add_f32_e32 v2, v51, v2
	v_exp_f32_e32 v62, v65
	v_add_f32_e32 v2, v52, v2
	v_exp_f32_e32 v37, v82
	v_add_f32_e32 v2, v57, v2
	v_exp_f32_e32 v42, v83
	v_add_f32_e32 v2, v58, v2
	v_exp_f32_e32 v43, v84
	v_add_f32_e32 v2, v62, v2
	v_exp_f32_e32 v49, v85
	v_add_f32_e32 v2, v37, v2
	v_exp_f32_e32 v50, v86
	v_add_f32_e32 v2, v42, v2
	v_exp_f32_e32 v55, v87
	v_add_f32_e32 v2, v43, v2
	v_exp_f32_e32 v56, v88
	v_add_f32_e32 v2, v49, v2
	v_exp_f32_e32 v61, v89
	v_add_f32_e32 v2, v50, v2
	v_exp_f32_e32 v36, v90
	v_add_f32_e32 v2, v55, v2
	v_exp_f32_e32 v39, v91
	v_add_f32_e32 v2, v56, v2
	v_exp_f32_e32 v40, v92
	v_add_f32_e32 v2, v61, v2
	v_add_f32_e32 v2, v36, v2
	v_add_f32_e32 v2, v39, v2
	v_add_f32_e32 v14, v40, v2
	v_exp_f32_e32 v48, v93
	v_cvt_pk_bf16_f32 v2, v33, v18
	v_cvt_pk_bf16_f32 v3, v19, v20
	v_cvt_pk_bf16_f32 v4, v21, v22
	v_cvt_pk_bf16_f32 v5, v23, v24
	s_bitcmp1_b32 s96, 0
	s_cbranch_scc1 .Latt_b3m
	s_waitcnt vmcnt(0)
.Latt_b3m:
	s_waitcnt vmcnt(12)
	s_barrier
	ds_read_b64_tr_b16 v[10:11], v195
	ds_read_b64_tr_b16 v[12:13], v195 offset:1024
	ds_read_b64_tr_b16 v[6:7], v196
	ds_read_b64_tr_b16 v[8:9], v196 offset:1024
	s_waitcnt lgkmcnt(0)
	s_nop 0
	v_add_f32_e32 v34, v48, v14
	v_mfma_f32_32x32x16_bf16 v[18:33], v[10:13], v[2:5], 0
	v_exp_f32_e32 v63, v94
	v_exp_f32_e32 v65, v95
	v_exp_f32_e32 v64, v96
	v_mfma_f32_32x32x16_bf16 v[2:17], v[6:9], v[2:5], 0
	v_exp_f32_e32 v70, v70
	v_add_f32_e32 v34, v63, v34
	v_cvt_pk_bf16_f32 v82, v119, v120
	v_cvt_pk_bf16_f32 v83, v121, v122
	v_cvt_pk_bf16_f32 v84, v123, v124
	v_cvt_pk_bf16_f32 v85, v125, v126
	ds_read_b64_tr_b16 v[90:91], v197
	ds_read_b64_tr_b16 v[92:93], v197 offset:1024
	ds_read_b64_tr_b16 v[86:87], v198
	ds_read_b64_tr_b16 v[88:89], v198 offset:1024
	s_waitcnt lgkmcnt(0)
	v_add_f32_e32 v34, v65, v34
	v_mfma_f32_32x32x16_bf16 v[18:33], v[90:93], v[82:85], v[18:33]
	v_add_f32_e32 v34, v64, v34
	v_add_f32_e32 v59, v70, v34
	ds_bpermute_b32 v60, v118, v59
	v_mfma_f32_32x32x16_bf16 v[2:17], v[86:89], v[82:85], v[2:17]
	s_and_b64 vcc, exec, s[72:73]
	s_mov_b64 s[4:5], -1
	s_cbranch_vccnz .LBB0_473
	s_lshl_b32 s90, s37, 1
	s_nop 0
	s_add_i32 m0, s75, 0x800
	s_nop 0
	s_mov_b64 s[4:5], 0
